# csr pass A reads 16 segment elements per pass (four 16-byte loads), validity masks built in vcc
# speedup vs baseline: 1.0167x; 1.0078x over previous
.Lpa_loop:
	global_load_dwordx4 v[26:29], v[10:11], off offset:-16
	global_load_dwordx4 v[30:33], v[10:11], off
	global_load_dwordx4 v[34:37], v[10:11], off offset:16
	global_load_dwordx4 v[40:43], v[10:11], off offset:32
	s_mov_b64 s[44:45], exec
	s_and_b64 vcc, exec, s[10:11]
	s_waitcnt vmcnt(0)
	s_cbranch_vccnz .Lpa_generic
	ds_write_b32 v22, v26
	v_lshlrev_b32_sdwa v26, v24, v26 dst_sel:DWORD dst_unused:UNUSED_PAD src0_sel:DWORD src1_sel:WORD_1
	ds_add_u32 v26, v23 offset:24848
	s_add_i32 s12, s3, 1
	v_cmp_lt_i32_e32 vcc, s12, v1
	s_mov_b64 exec, vcc
	ds_write_b32 v22, v27 offset:4
	v_lshlrev_b32_sdwa v27, v24, v27 dst_sel:DWORD dst_unused:UNUSED_PAD src0_sel:DWORD src1_sel:WORD_1
	ds_add_u32 v27, v23 offset:24848
	s_add_i32 s12, s3, 2
	v_cmp_lt_i32_e32 vcc, s12, v1
	s_mov_b64 exec, vcc
	ds_write_b32 v22, v28 offset:8
	v_lshlrev_b32_sdwa v28, v24, v28 dst_sel:DWORD dst_unused:UNUSED_PAD src0_sel:DWORD src1_sel:WORD_1
	ds_add_u32 v28, v23 offset:24848
	s_add_i32 s12, s3, 3
	v_cmp_lt_i32_e32 vcc, s12, v1
	s_mov_b64 exec, vcc
	ds_write_b32 v22, v29 offset:12
	v_lshlrev_b32_sdwa v29, v24, v29 dst_sel:DWORD dst_unused:UNUSED_PAD src0_sel:DWORD src1_sel:WORD_1
	ds_add_u32 v29, v23 offset:24848
	s_add_i32 s12, s3, 4
	v_cmp_lt_i32_e32 vcc, s12, v1
	s_mov_b64 exec, vcc
	ds_write_b32 v22, v30 offset:16
	v_lshlrev_b32_sdwa v30, v24, v30 dst_sel:DWORD dst_unused:UNUSED_PAD src0_sel:DWORD src1_sel:WORD_1
	ds_add_u32 v30, v23 offset:24848
	s_add_i32 s12, s3, 5
	v_cmp_lt_i32_e32 vcc, s12, v1
	s_mov_b64 exec, vcc
	ds_write_b32 v22, v31 offset:20
	v_lshlrev_b32_sdwa v31, v24, v31 dst_sel:DWORD dst_unused:UNUSED_PAD src0_sel:DWORD src1_sel:WORD_1
	ds_add_u32 v31, v23 offset:24848
	s_add_i32 s12, s3, 6
	v_cmp_lt_i32_e32 vcc, s12, v1
	s_mov_b64 exec, vcc
	ds_write_b32 v22, v32 offset:24
	v_lshlrev_b32_sdwa v32, v24, v32 dst_sel:DWORD dst_unused:UNUSED_PAD src0_sel:DWORD src1_sel:WORD_1
	ds_add_u32 v32, v23 offset:24848
	s_add_i32 s12, s3, 7
	v_cmp_lt_i32_e32 vcc, s12, v1
	s_mov_b64 exec, vcc
	ds_write_b32 v22, v33 offset:28
	v_lshlrev_b32_sdwa v33, v24, v33 dst_sel:DWORD dst_unused:UNUSED_PAD src0_sel:DWORD src1_sel:WORD_1
	ds_add_u32 v33, v23 offset:24848
	s_add_i32 s12, s3, 8
	v_cmp_lt_i32_e32 vcc, s12, v1
	s_mov_b64 exec, vcc
	ds_write_b32 v22, v34 offset:32
	v_lshlrev_b32_sdwa v34, v24, v34 dst_sel:DWORD dst_unused:UNUSED_PAD src0_sel:DWORD src1_sel:WORD_1
	ds_add_u32 v34, v23 offset:24848
	s_add_i32 s12, s3, 9
	v_cmp_lt_i32_e32 vcc, s12, v1
	s_mov_b64 exec, vcc
	ds_write_b32 v22, v35 offset:36
	v_lshlrev_b32_sdwa v35, v24, v35 dst_sel:DWORD dst_unused:UNUSED_PAD src0_sel:DWORD src1_sel:WORD_1
	ds_add_u32 v35, v23 offset:24848
	s_add_i32 s12, s3, 10
	v_cmp_lt_i32_e32 vcc, s12, v1
	s_mov_b64 exec, vcc
	ds_write_b32 v22, v36 offset:40
	v_lshlrev_b32_sdwa v36, v24, v36 dst_sel:DWORD dst_unused:UNUSED_PAD src0_sel:DWORD src1_sel:WORD_1
	ds_add_u32 v36, v23 offset:24848
	s_add_i32 s12, s3, 11
	v_cmp_lt_i32_e32 vcc, s12, v1
	s_mov_b64 exec, vcc
	ds_write_b32 v22, v37 offset:44
	v_lshlrev_b32_sdwa v37, v24, v37 dst_sel:DWORD dst_unused:UNUSED_PAD src0_sel:DWORD src1_sel:WORD_1
	ds_add_u32 v37, v23 offset:24848
	s_add_i32 s12, s3, 12
	v_cmp_lt_i32_e32 vcc, s12, v1
	s_mov_b64 exec, vcc
	ds_write_b32 v22, v40 offset:48
	v_lshlrev_b32_sdwa v40, v24, v40 dst_sel:DWORD dst_unused:UNUSED_PAD src0_sel:DWORD src1_sel:WORD_1
	ds_add_u32 v40, v23 offset:24848
	s_add_i32 s12, s3, 13
	v_cmp_lt_i32_e32 vcc, s12, v1
	s_mov_b64 exec, vcc
	ds_write_b32 v22, v41 offset:52
	v_lshlrev_b32_sdwa v41, v24, v41 dst_sel:DWORD dst_unused:UNUSED_PAD src0_sel:DWORD src1_sel:WORD_1
	ds_add_u32 v41, v23 offset:24848
	s_add_i32 s12, s3, 14
	v_cmp_lt_i32_e32 vcc, s12, v1
	s_mov_b64 exec, vcc
	ds_write_b32 v22, v42 offset:56
	v_lshlrev_b32_sdwa v42, v24, v42 dst_sel:DWORD dst_unused:UNUSED_PAD src0_sel:DWORD src1_sel:WORD_1
	ds_add_u32 v42, v23 offset:24848
	s_add_i32 s12, s3, 15
	v_cmp_lt_i32_e32 vcc, s12, v1
	s_mov_b64 exec, vcc
	ds_write_b32 v22, v43 offset:60
	v_lshlrev_b32_sdwa v43, v24, v43 dst_sel:DWORD dst_unused:UNUSED_PAD src0_sel:DWORD src1_sel:WORD_1
	ds_add_u32 v43, v23 offset:24848
	s_branch .Lpa_next
.Lpa_generic:
	v_lshlrev_b32_sdwa v26, v24, v26 dst_sel:DWORD dst_unused:UNUSED_PAD src0_sel:DWORD src1_sel:WORD_1
	ds_add_u32 v26, v23 offset:24848
	s_add_i32 s12, s3, 1
	v_cmp_lt_i32_e32 vcc, s12, v1
	s_mov_b64 exec, vcc
	v_lshlrev_b32_sdwa v27, v24, v27 dst_sel:DWORD dst_unused:UNUSED_PAD src0_sel:DWORD src1_sel:WORD_1
	ds_add_u32 v27, v23 offset:24848
	s_add_i32 s12, s3, 2
	v_cmp_lt_i32_e32 vcc, s12, v1
	s_mov_b64 exec, vcc
	v_lshlrev_b32_sdwa v28, v24, v28 dst_sel:DWORD dst_unused:UNUSED_PAD src0_sel:DWORD src1_sel:WORD_1
	ds_add_u32 v28, v23 offset:24848
	s_add_i32 s12, s3, 3
	v_cmp_lt_i32_e32 vcc, s12, v1
	s_mov_b64 exec, vcc
	v_lshlrev_b32_sdwa v29, v24, v29 dst_sel:DWORD dst_unused:UNUSED_PAD src0_sel:DWORD src1_sel:WORD_1
	ds_add_u32 v29, v23 offset:24848
	s_add_i32 s12, s3, 4
	v_cmp_lt_i32_e32 vcc, s12, v1
	s_mov_b64 exec, vcc
	v_lshlrev_b32_sdwa v30, v24, v30 dst_sel:DWORD dst_unused:UNUSED_PAD src0_sel:DWORD src1_sel:WORD_1
	ds_add_u32 v30, v23 offset:24848
	s_add_i32 s12, s3, 5
	v_cmp_lt_i32_e32 vcc, s12, v1
	s_mov_b64 exec, vcc
	v_lshlrev_b32_sdwa v31, v24, v31 dst_sel:DWORD dst_unused:UNUSED_PAD src0_sel:DWORD src1_sel:WORD_1
	ds_add_u32 v31, v23 offset:24848
	s_add_i32 s12, s3, 6
	v_cmp_lt_i32_e32 vcc, s12, v1
	s_mov_b64 exec, vcc
	v_lshlrev_b32_sdwa v32, v24, v32 dst_sel:DWORD dst_unused:UNUSED_PAD src0_sel:DWORD src1_sel:WORD_1
	ds_add_u32 v32, v23 offset:24848
	s_add_i32 s12, s3, 7
	v_cmp_lt_i32_e32 vcc, s12, v1
	s_mov_b64 exec, vcc
	v_lshlrev_b32_sdwa v33, v24, v33 dst_sel:DWORD dst_unused:UNUSED_PAD src0_sel:DWORD src1_sel:WORD_1
	ds_add_u32 v33, v23 offset:24848
	s_add_i32 s12, s3, 8
	v_cmp_lt_i32_e32 vcc, s12, v1
	s_mov_b64 exec, vcc
	v_lshlrev_b32_sdwa v34, v24, v34 dst_sel:DWORD dst_unused:UNUSED_PAD src0_sel:DWORD src1_sel:WORD_1
	ds_add_u32 v34, v23 offset:24848
	s_add_i32 s12, s3, 9
	v_cmp_lt_i32_e32 vcc, s12, v1
	s_mov_b64 exec, vcc
	v_lshlrev_b32_sdwa v35, v24, v35 dst_sel:DWORD dst_unused:UNUSED_PAD src0_sel:DWORD src1_sel:WORD_1
	ds_add_u32 v35, v23 offset:24848
	s_add_i32 s12, s3, 10
	v_cmp_lt_i32_e32 vcc, s12, v1
	s_mov_b64 exec, vcc
	v_lshlrev_b32_sdwa v36, v24, v36 dst_sel:DWORD dst_unused:UNUSED_PAD src0_sel:DWORD src1_sel:WORD_1
	ds_add_u32 v36, v23 offset:24848
	s_add_i32 s12, s3, 11
	v_cmp_lt_i32_e32 vcc, s12, v1
	s_mov_b64 exec, vcc
	v_lshlrev_b32_sdwa v37, v24, v37 dst_sel:DWORD dst_unused:UNUSED_PAD src0_sel:DWORD src1_sel:WORD_1
	ds_add_u32 v37, v23 offset:24848
	s_add_i32 s12, s3, 12
	v_cmp_lt_i32_e32 vcc, s12, v1
	s_mov_b64 exec, vcc
	v_lshlrev_b32_sdwa v40, v24, v40 dst_sel:DWORD dst_unused:UNUSED_PAD src0_sel:DWORD src1_sel:WORD_1
	ds_add_u32 v40, v23 offset:24848
	s_add_i32 s12, s3, 13
	v_cmp_lt_i32_e32 vcc, s12, v1
	s_mov_b64 exec, vcc
	v_lshlrev_b32_sdwa v41, v24, v41 dst_sel:DWORD dst_unused:UNUSED_PAD src0_sel:DWORD src1_sel:WORD_1
	ds_add_u32 v41, v23 offset:24848
	s_add_i32 s12, s3, 14
	v_cmp_lt_i32_e32 vcc, s12, v1
	s_mov_b64 exec, vcc
	v_lshlrev_b32_sdwa v42, v24, v42 dst_sel:DWORD dst_unused:UNUSED_PAD src0_sel:DWORD src1_sel:WORD_1
	ds_add_u32 v42, v23 offset:24848
	s_add_i32 s12, s3, 15
	v_cmp_lt_i32_e32 vcc, s12, v1
	s_mov_b64 exec, vcc
	v_lshlrev_b32_sdwa v43, v24, v43 dst_sel:DWORD dst_unused:UNUSED_PAD src0_sel:DWORD src1_sel:WORD_1
	ds_add_u32 v43, v23 offset:24848
.Lpa_next:
	s_mov_b64 exec, s[44:45]
	s_add_i32 s3, s3, 16
	v_cmp_ge_i32_e32 vcc, s3, v1
	v_add_u32_e32 v22, 64, v22
	s_or_b64 s[42:43], vcc, s[42:43]
	v_lshl_add_u64 v[10:11], v[10:11], 0, 64
	s_andn2_b64 exec, exec, s[42:43]
	s_cbranch_execnz .Lpa_loop
